# global attention loop: row-sum chains via v_pk_add_f32 pairs (18 instead of 32 adds per half tile)
# baseline (speedup 1.0000x reference)
.LBB0_593:
	ds_read_b128 v[80:83], v212 offset:49152
	ds_read_b128 v[84:87], v212 offset:57344
	ds_read_b128 v[160:163], v211 offset:49152
	ds_read_b128 v[164:167], v211 offset:57344
	v_exp_f32_e32 v168, v72
	v_exp_f32_e32 v169, v73
	s_waitcnt lgkmcnt(3)
	v_mfma_f32_32x32x16_bf16 v[96:111], v[80:83], v[140:143], 0
	v_exp_f32_e32 v170, v74
	v_exp_f32_e32 v171, v75
	v_exp_f32_e32 v172, v76
	v_exp_f32_e32 v173, v77
	v_exp_f32_e32 v174, v78
	v_exp_f32_e32 v79, v79
	s_waitcnt lgkmcnt(2)
	v_mfma_f32_32x32x16_bf16 v[80:95], v[84:87], v[140:143], 0
	s_waitcnt lgkmcnt(1)
	v_mfma_f32_32x32x16_bf16 v[96:111], v[160:163], v[136:139], v[96:111]
	s_waitcnt lgkmcnt(0)
	v_mfma_f32_32x32x16_bf16 v[80:95], v[164:167], v[136:139], v[80:95]
	ds_read_b128 v[160:163], v210 offset:49152
	ds_read_b128 v[164:167], v210 offset:57344
	s_waitcnt lgkmcnt(1)
	v_mfma_f32_32x32x16_bf16 v[96:111], v[160:163], v[132:135], v[96:111]
	s_waitcnt lgkmcnt(0)
	v_mfma_f32_32x32x16_bf16 v[80:95], v[164:167], v[132:135], v[80:95]
	ds_read_b128 v[160:163], v209 offset:49152
	ds_read_b128 v[164:167], v209 offset:57344
	s_waitcnt lgkmcnt(1)
	v_mfma_f32_32x32x16_bf16 v[96:111], v[160:163], v[128:131], v[96:111]
	s_waitcnt lgkmcnt(0)
	v_mfma_f32_32x32x16_bf16 v[80:95], v[164:167], v[128:131], v[80:95]
	ds_read_b128 v[160:163], v208 offset:49152
	ds_read_b128 v[164:167], v208 offset:57344
	s_waitcnt lgkmcnt(1)
	v_mfma_f32_32x32x16_bf16 v[96:111], v[160:163], v[124:127], v[96:111]
	s_waitcnt lgkmcnt(0)
	v_mfma_f32_32x32x16_bf16 v[80:95], v[164:167], v[124:127], v[80:95]
	ds_read_b128 v[160:163], v213 offset:49152
	ds_read_b128 v[164:167], v213 offset:57344
	s_waitcnt lgkmcnt(1)
	v_mfma_f32_32x32x16_bf16 v[96:111], v[160:163], v[120:123], v[96:111]
	s_waitcnt lgkmcnt(0)
	v_mfma_f32_32x32x16_bf16 v[80:95], v[164:167], v[120:123], v[80:95]
	ds_read_b128 v[160:163], v214 offset:49152
	ds_read_b128 v[164:167], v214 offset:57344
	s_waitcnt lgkmcnt(1)
	v_mfma_f32_32x32x16_bf16 v[96:111], v[160:163], v[116:119], v[96:111]
	s_waitcnt lgkmcnt(0)
	v_mfma_f32_32x32x16_bf16 v[80:95], v[164:167], v[116:119], v[80:95]
	ds_read_b128 v[160:163], v215 offset:49152
	ds_read_b128 v[164:167], v215 offset:57344
	s_waitcnt lgkmcnt(1)
	v_mfma_f32_32x32x16_bf16 v[96:111], v[160:163], v[112:115], v[96:111]
	v_exp_f32_e32 v160, v64
	v_exp_f32_e32 v161, v65
	v_pk_add_f32 v[64:65], v[222:223], v[224:225]
	v_pk_add_f32 v[64:65], v[64:65], v[226:227]
	v_pk_add_f32 v[64:65], v[64:65], v[228:229]
	v_pk_add_f32 v[64:65], v[64:65], v[230:231]
	v_pk_add_f32 v[64:65], v[64:65], v[232:233]
	v_pk_add_f32 v[64:65], v[64:65], v[188:189]
	v_exp_f32_e32 v162, v66
	v_pk_add_f32 v[64:65], v[64:65], v[190:191]
	v_exp_f32_e32 v163, v67
	v_pk_add_f32 v[64:65], v[64:65], v[168:169]
	v_pk_add_f32 v[64:65], v[64:65], v[170:171]
	s_waitcnt lgkmcnt(0)
	v_mfma_f32_32x32x16_bf16 v[80:95], v[164:167], v[112:115], v[80:95]
	v_exp_f32_e32 v164, v68
	v_pk_add_f32 v[64:65], v[64:65], v[172:173]
	v_exp_f32_e32 v165, v69
	v_pk_add_f32 v[64:65], v[64:65], v[160:161]
	v_exp_f32_e32 v166, v70
	v_pk_add_f32 v[64:65], v[64:65], v[162:163]
	v_exp_f32_e32 v167, v71
	v_pk_add_f32 v[64:65], v[64:65], v[164:165]
	v_pk_add_f32 v[64:65], v[64:65], v[166:167]
	v_add_f32_e32 v64, v64, v65
	v_add_f32_e32 v64, v174, v64
	v_add_f32_e32 v234, v79, v64
	v_cvt_pk_bf16_f32 v64, v231, v233
	v_cvt_pk_bf16_f32 v65, v229, v232
	v_cvt_pk_bf16_f32 v66, v228, v230
	v_cvt_pk_bf16_f32 v67, v226, v227
	v_cvt_pk_bf16_f32 v68, v223, v225
	v_cvt_pk_bf16_f32 v69, v222, v224
	v_cvt_pk_bf16_f32 v70, v188, v191
	v_cvt_pk_bf16_f32 v71, v189, v190
	v_cvt_pk_bf16_f32 v72, v160, v161
	v_cvt_pk_bf16_f32 v73, v162, v163
	v_cvt_pk_bf16_f32 v74, v164, v165
	v_cvt_pk_bf16_f32 v75, v166, v167
	v_cvt_pk_bf16_f32 v76, v168, v169
	v_cvt_pk_bf16_f32 v77, v170, v171
	v_cvt_pk_bf16_f32 v78, v172, v173
	v_cvt_pk_bf16_f32 v79, v174, v79
	s_nop 1
	v_permlane32_swap_b32_e32 v64, v66
	v_permlane32_swap_b32_e32 v65, v67
	v_permlane32_swap_b32_e32 v68, v70
	v_permlane32_swap_b32_e32 v69, v71
	v_permlane32_swap_b32_e32 v72, v74
	v_permlane32_swap_b32_e32 v73, v75
	v_permlane32_swap_b32_e32 v76, v78
	v_permlane32_swap_b32_e32 v77, v79
	v_lshl_add_u64 v[196:197], v[196:197], 0, s[100:101]
	v_lshl_add_u64 v[198:199], v[198:199], 0, s[100:101]
	global_load_dwordx4 v[160:163], v[196:197], off offset:2560
	global_load_dwordx4 v[164:167], v[196:197], off offset:2048
	global_load_dwordx4 v[172:175], v[198:199], off offset:2560
	global_load_dwordx4 v[168:171], v[198:199], off offset:2048
	ds_read_b64_tr_b16 v[222:223], v185 offset:0
	ds_read_b64_tr_b16 v[224:225], v185 offset:0x800
	ds_read_b64_tr_b16 v[226:227], v185 offset:0x1000
	ds_read_b64_tr_b16 v[228:229], v185 offset:0x1800
	ds_read_b64_tr_b16 v[230:231], v185 offset:0x2000
	ds_read_b64_tr_b16 v[232:233], v185 offset:0x2800
	ds_read_b64_tr_b16 v[236:237], v185 offset:0x3000
	ds_read_b64_tr_b16 v[238:239], v185 offset:0x3800
	s_waitcnt lgkmcnt(6)
	s_nop 0
	v_mfma_f32_32x32x16_bf16 v[0:15], v[64:67], v[222:225], v[0:15]
	ds_read_b64_tr_b16 v[222:223], v185 offset:0x200
	ds_read_b64_tr_b16 v[224:225], v185 offset:0xa00
	s_waitcnt lgkmcnt(6)
	v_mfma_f32_32x32x16_bf16 v[0:15], v[68:71], v[226:229], v[0:15]
	ds_read_b64_tr_b16 v[226:227], v185 offset:0x1200
	ds_read_b64_tr_b16 v[228:229], v185 offset:0x1a00
	s_waitcnt lgkmcnt(6)
	v_mfma_f32_32x32x16_bf16 v[0:15], v[72:75], v[230:233], v[0:15]
	ds_read_b64_tr_b16 v[230:231], v185 offset:0x2200
	ds_read_b64_tr_b16 v[232:233], v185 offset:0x2a00
	s_waitcnt lgkmcnt(6)
	v_mfma_f32_32x32x16_bf16 v[0:15], v[76:79], v[236:239], v[0:15]
	ds_read_b64_tr_b16 v[236:237], v185 offset:0x3200
	ds_read_b64_tr_b16 v[238:239], v185 offset:0x3a00
	s_waitcnt lgkmcnt(6)
	v_mfma_f32_32x32x16_bf16 v[16:31], v[64:67], v[222:225], v[16:31]
	ds_read_b64_tr_b16 v[222:223], v185 offset:0x400
	ds_read_b64_tr_b16 v[224:225], v185 offset:0xc00
	s_waitcnt lgkmcnt(6)
	v_mfma_f32_32x32x16_bf16 v[16:31], v[68:71], v[226:229], v[16:31]
	ds_read_b64_tr_b16 v[226:227], v185 offset:0x1400
	ds_read_b64_tr_b16 v[228:229], v185 offset:0x1c00
	s_waitcnt lgkmcnt(6)
	v_mfma_f32_32x32x16_bf16 v[16:31], v[72:75], v[230:233], v[16:31]
	ds_read_b64_tr_b16 v[230:231], v185 offset:0x2400
	ds_read_b64_tr_b16 v[232:233], v185 offset:0x2c00
	s_waitcnt lgkmcnt(6)
	v_mfma_f32_32x32x16_bf16 v[16:31], v[76:79], v[236:239], v[16:31]
	ds_read_b64_tr_b16 v[236:237], v185 offset:0x3400
	ds_read_b64_tr_b16 v[238:239], v185 offset:0x3c00
	s_waitcnt lgkmcnt(6)
	v_mfma_f32_32x32x16_bf16 v[32:47], v[64:67], v[222:225], v[32:47]
	ds_read_b64_tr_b16 v[222:223], v185 offset:0x600
	ds_read_b64_tr_b16 v[224:225], v185 offset:0xe00
	s_waitcnt vmcnt(4)
	ds_write_b128 v206, v[148:151] offset:32768
	ds_write_b128 v207, v[156:159] offset:32768
	s_waitcnt lgkmcnt(8)
	v_mfma_f32_32x32x16_bf16 v[32:47], v[68:71], v[226:229], v[32:47]
	ds_read_b64_tr_b16 v[226:227], v185 offset:0x1600
	ds_read_b64_tr_b16 v[228:229], v185 offset:0x1e00
	s_waitcnt lgkmcnt(8)
	v_mfma_f32_32x32x16_bf16 v[32:47], v[72:75], v[230:233], v[32:47]
	ds_read_b64_tr_b16 v[230:231], v185 offset:0x2600
	ds_read_b64_tr_b16 v[232:233], v185 offset:0x2e00
	s_waitcnt lgkmcnt(8)
	v_mfma_f32_32x32x16_bf16 v[32:47], v[76:79], v[236:239], v[32:47]
	ds_read_b64_tr_b16 v[236:237], v185 offset:0x3600
	ds_read_b64_tr_b16 v[238:239], v185 offset:0x3e00
	s_waitcnt lgkmcnt(8)
	v_mfma_f32_32x32x16_bf16 v[48:63], v[64:67], v[222:225], v[48:63]
	s_waitcnt lgkmcnt(0)
	s_barrier
	s_waitcnt vmcnt(4)
	v_exp_f32_e32 v218, v96
	v_exp_f32_e32 v219, v97
	v_exp_f32_e32 v220, v98
	v_mfma_f32_32x32x16_bf16 v[48:63], v[68:71], v[226:229], v[48:63]
	v_exp_f32_e32 v221, v99
	v_exp_f32_e32 v240, v108
	v_exp_f32_e32 v241, v109
	v_exp_f32_e32 v242, v110
	v_exp_f32_e32 v243, v111
	s_waitcnt vmcnt(7)
	ds_write_b128 v204, v[144:147]
	s_waitcnt vmcnt(6)
	ds_write_b128 v205, v[152:155]
	v_mfma_f32_32x32x16_bf16 v[48:63], v[72:75], v[230:233], v[48:63]
	v_exp_f32_e32 v230, v100
	v_exp_f32_e32 v231, v101
	v_exp_f32_e32 v232, v102
	v_exp_f32_e32 v233, v103
	v_mfma_f32_32x32x16_bf16 v[48:63], v[76:79], v[236:239], v[48:63]
	v_exp_f32_e32 v236, v104
	v_exp_f32_e32 v237, v105
	v_exp_f32_e32 v238, v106
	v_exp_f32_e32 v239, v107
	ds_read_b128 v[64:67], v212 offset:32768
	ds_read_b128 v[68:71], v212 offset:40960
	ds_read_b128 v[222:225], v211 offset:32768
	ds_read_b128 v[226:229], v211 offset:40960
	v_exp_f32_e32 v244, v86
	v_exp_f32_e32 v245, v87
	s_waitcnt lgkmcnt(3)
	v_mfma_f32_32x32x16_bf16 v[96:111], v[64:67], v[140:143], 0
	v_exp_f32_e32 v246, v88
	v_exp_f32_e32 v247, v89
	v_exp_f32_e32 v248, v90
	v_exp_f32_e32 v249, v91
	v_exp_f32_e32 v250, v92
	v_exp_f32_e32 v251, v93
	v_exp_f32_e32 v252, v94
	s_waitcnt lgkmcnt(2)
	v_mfma_f32_32x32x16_bf16 v[64:79], v[68:71], v[140:143], 0
	v_exp_f32_e32 v95, v95
	s_waitcnt lgkmcnt(1)
	v_mfma_f32_32x32x16_bf16 v[96:111], v[222:225], v[136:139], v[96:111]
	s_waitcnt lgkmcnt(0)
	v_mfma_f32_32x32x16_bf16 v[64:79], v[226:229], v[136:139], v[64:79]
	ds_read_b128 v[222:225], v210 offset:32768
	ds_read_b128 v[226:229], v210 offset:40960
	s_waitcnt lgkmcnt(1)
	v_mfma_f32_32x32x16_bf16 v[96:111], v[222:225], v[132:135], v[96:111]
	s_waitcnt lgkmcnt(0)
	v_mfma_f32_32x32x16_bf16 v[64:79], v[226:229], v[132:135], v[64:79]
	ds_read_b128 v[222:225], v209 offset:32768
	ds_read_b128 v[226:229], v209 offset:40960
	s_waitcnt lgkmcnt(1)
	v_mfma_f32_32x32x16_bf16 v[96:111], v[222:225], v[128:131], v[96:111]
	s_waitcnt lgkmcnt(0)
	v_mfma_f32_32x32x16_bf16 v[64:79], v[226:229], v[128:131], v[64:79]
	ds_read_b128 v[222:225], v208 offset:32768
	ds_read_b128 v[226:229], v208 offset:40960
	s_waitcnt lgkmcnt(1)
	v_mfma_f32_32x32x16_bf16 v[96:111], v[222:225], v[124:127], v[96:111]
	s_waitcnt lgkmcnt(0)
	v_mfma_f32_32x32x16_bf16 v[64:79], v[226:229], v[124:127], v[64:79]
	ds_read_b128 v[222:225], v213 offset:32768
	ds_read_b128 v[226:229], v213 offset:40960
	s_waitcnt lgkmcnt(1)
	v_mfma_f32_32x32x16_bf16 v[96:111], v[222:225], v[120:123], v[96:111]
	s_waitcnt lgkmcnt(0)
	v_mfma_f32_32x32x16_bf16 v[64:79], v[226:229], v[120:123], v[64:79]
	ds_read_b128 v[222:225], v214 offset:32768
	ds_read_b128 v[226:229], v214 offset:40960
	s_waitcnt lgkmcnt(1)
	v_mfma_f32_32x32x16_bf16 v[96:111], v[222:225], v[116:119], v[96:111]
	s_waitcnt lgkmcnt(0)
	v_mfma_f32_32x32x16_bf16 v[64:79], v[226:229], v[116:119], v[64:79]
	ds_read_b128 v[222:225], v215 offset:32768
	ds_read_b128 v[226:229], v215 offset:40960
	s_waitcnt lgkmcnt(1)
	v_mfma_f32_32x32x16_bf16 v[96:111], v[222:225], v[112:115], v[96:111]
	v_exp_f32_e32 v224, v80
	v_exp_f32_e32 v225, v81
	v_pk_add_f32 v[80:81], v[218:219], v[220:221]
	v_pk_add_f32 v[80:81], v[80:81], v[230:231]
	v_pk_add_f32 v[80:81], v[80:81], v[232:233]
	v_pk_add_f32 v[80:81], v[80:81], v[236:237]
	v_pk_add_f32 v[80:81], v[80:81], v[238:239]
	v_pk_add_f32 v[80:81], v[80:81], v[240:241]
	v_pk_add_f32 v[80:81], v[80:81], v[242:243]
	v_pk_add_f32 v[80:81], v[80:81], v[244:245]
	v_pk_add_f32 v[80:81], v[80:81], v[246:247]
	s_waitcnt lgkmcnt(0)
	v_mfma_f32_32x32x16_bf16 v[64:79], v[226:229], v[112:115], v[64:79]
	v_exp_f32_e32 v226, v82
	v_pk_add_f32 v[80:81], v[80:81], v[248:249]
	v_exp_f32_e32 v227, v83
	v_pk_add_f32 v[80:81], v[80:81], v[250:251]
	v_exp_f32_e32 v228, v84
	v_pk_add_f32 v[80:81], v[80:81], v[224:225]
	v_exp_f32_e32 v229, v85
	v_pk_add_f32 v[80:81], v[80:81], v[226:227]
	v_pk_add_f32 v[80:81], v[80:81], v[228:229]
	v_add_f32_e32 v80, v80, v81
	v_add_f32_e32 v80, v252, v80
	v_add_f32_e32 v222, v95, v80
	v_cvt_pk_bf16_f32 v80, v218, v219
	v_cvt_pk_bf16_f32 v81, v220, v221
	v_cvt_pk_bf16_f32 v82, v230, v231
	v_cvt_pk_bf16_f32 v83, v232, v233
	v_cvt_pk_bf16_f32 v84, v236, v237
	v_cvt_pk_bf16_f32 v85, v238, v239
	v_cvt_pk_bf16_f32 v86, v240, v241
	v_cvt_pk_bf16_f32 v87, v242, v243
	v_cvt_pk_bf16_f32 v88, v224, v225
	v_cvt_pk_bf16_f32 v89, v226, v227
	v_cvt_pk_bf16_f32 v90, v228, v229
	v_cvt_pk_bf16_f32 v91, v244, v245
	v_cvt_pk_bf16_f32 v92, v246, v247
	v_cvt_pk_bf16_f32 v93, v248, v249
	v_cvt_pk_bf16_f32 v94, v250, v251
	v_cvt_pk_bf16_f32 v95, v252, v95
	s_nop 1
	v_permlane32_swap_b32_e32 v80, v82
	v_permlane32_swap_b32_e32 v81, v83
	v_permlane32_swap_b32_e32 v84, v86
	v_permlane32_swap_b32_e32 v85, v87
	v_permlane32_swap_b32_e32 v88, v90
	v_permlane32_swap_b32_e32 v89, v91
	v_permlane32_swap_b32_e32 v92, v94
	v_permlane32_swap_b32_e32 v93, v95
	s_cmp_gt_u32 s8, s29
	s_cselect_b64 s[6:7], -1, 0
	v_lshl_add_u64 v[196:197], v[196:197], 0, s[100:101]
	v_lshl_add_u64 v[198:199], v[198:199], 0, s[100:101]
	global_load_dwordx4 v[144:147], v[196:197], off offset:2560
	global_load_dwordx4 v[148:151], v[196:197], off offset:2048
	global_load_dwordx4 v[152:155], v[198:199], off offset:2560
	global_load_dwordx4 v[156:159], v[198:199], off offset:2048
	s_branch .LBB0_592
